# stack10 + attention tile loop edge: counter, DMA pointer bumps and bias index update moved from after the per-tile barrier to before it (same code size)
# speedup vs baseline: 1.0021x; 1.0021x over previous
; __device__ __forceinline__ void attn_unit(LAS unsigned char* lds, const bf16* proj, bf16* Y, const float* relb, const float* hgain, float lam, float oscale, int b, int h, int qb, int tid, int lane, int wid, Stopwatch& sw) {
;     ...
;     for (int t = 0; t < NT; ++t) ATT_TILE(t);
.LBB0_439:
	s_add_i32 s72, s72, 1
	v_lshl_add_u64 v[154:155], v[154:155], 0, s[92:93]
	v_lshl_add_u64 v[156:157], v[156:157], 0, s[92:93]
	v_lshl_add_u64 v[158:159], v[158:159], 0, s[92:93]
	v_lshl_add_u64 v[160:161], v[160:161], 0, s[92:93]
	v_subrev_u32_e32 v176, 64, v176
	s_waitcnt vmcnt(0) lgkmcnt(0)
	s_barrier
	s_cmp_eq_u32 s5, s34
	s_cbranch_scc0 .LBB0_395
	s_lshl_b32 s0, s19, 6
	s_add_i32 s0, s0, 64
	s_cmp_gt_u32 s0, s24
	s_cbranch_scc1 .LBB0_442
	v_add_u32_e32 v100, s82, v175
	v_add_u32_e32 v101, s82, v174
	v_add_u32_e32 v102, s82, v173
	v_add_u32_e32 v103, s82, v172
	v_add_u32_e32 v104, s82, v171
	v_add_u32_e32 v105, s82, v170
	v_add_u32_e32 v106, s82, v169
	v_add_u32_e32 v107, s82, v168
	ds_read_b64_tr_b16 v[68:69], v100 offset:16384
	ds_read_b64_tr_b16 v[70:71], v101 offset:16384
	ds_read_b64_tr_b16 v[74:75], v101 offset:20480
	ds_read_b64_tr_b16 v[72:73], v100 offset:20480
	ds_read_b64_tr_b16 v[76:77], v102 offset:16384
	ds_read_b64_tr_b16 v[78:79], v103 offset:16384
	ds_read_b64_tr_b16 v[82:83], v103 offset:20480
	ds_read_b64_tr_b16 v[80:81], v102 offset:20480
	ds_read_b64_tr_b16 v[84:85], v104 offset:16384
	ds_read_b64_tr_b16 v[86:87], v105 offset:16384
	ds_read_b64_tr_b16 v[90:91], v105 offset:20480
	ds_read_b64_tr_b16 v[88:89], v104 offset:20480
	ds_read_b64_tr_b16 v[92:93], v106 offset:16384
	ds_read_b64_tr_b16 v[94:95], v107 offset:16384
	ds_read_b64_tr_b16 v[98:99], v107 offset:20480
	ds_read_b64_tr_b16 v[96:97], v106 offset:20480
	s_waitcnt lgkmcnt(14)
	v_mfma_f32_32x32x16_bf16 v[52:67], v[68:71], v[144:147], v[52:67]
	s_waitcnt lgkmcnt(10)
	v_mfma_f32_32x32x16_bf16 v[36:51], v[76:79], v[144:147], v[36:51]
	s_waitcnt lgkmcnt(6)
	v_mfma_f32_32x32x16_bf16 v[20:35], v[84:87], v[144:147], v[20:35]
	s_waitcnt lgkmcnt(2)
	v_mfma_f32_32x32x16_bf16 v[4:19], v[92:95], v[144:147], v[4:19]
	ds_read_b64_tr_b16 v[68:69], v100 offset:24576
	ds_read_b64_tr_b16 v[70:71], v101 offset:24576
	ds_read_b64_tr_b16 v[76:77], v102 offset:24576
	ds_read_b64_tr_b16 v[78:79], v103 offset:24576
	ds_read_b64_tr_b16 v[84:85], v104 offset:24576
	ds_read_b64_tr_b16 v[86:87], v105 offset:24576
	ds_read_b64_tr_b16 v[92:93], v106 offset:24576
	ds_read_b64_tr_b16 v[94:95], v107 offset:24576
	v_mfma_f32_32x32x16_bf16 v[52:67], v[72:75], v[140:143], v[52:67]
	v_mfma_f32_32x32x16_bf16 v[36:51], v[80:83], v[140:143], v[36:51]
	v_mfma_f32_32x32x16_bf16 v[20:35], v[88:91], v[140:143], v[20:35]
	s_waitcnt lgkmcnt(8)
	v_mfma_f32_32x32x16_bf16 v[4:19], v[96:99], v[140:143], v[4:19]
	ds_read_b64_tr_b16 v[72:73], v100 offset:28672
	ds_read_b64_tr_b16 v[74:75], v101 offset:28672
	ds_read_b64_tr_b16 v[80:81], v102 offset:28672
	ds_read_b64_tr_b16 v[82:83], v103 offset:28672
	ds_read_b64_tr_b16 v[88:89], v104 offset:28672
	ds_read_b64_tr_b16 v[90:91], v105 offset:28672
	ds_read_b64_tr_b16 v[96:97], v106 offset:28672
	ds_read_b64_tr_b16 v[98:99], v107 offset:28672
	s_waitcnt lgkmcnt(14)
	v_mfma_f32_32x32x16_bf16 v[52:67], v[68:71], v[132:135], v[52:67]
	s_waitcnt lgkmcnt(12)
	v_mfma_f32_32x32x16_bf16 v[36:51], v[76:79], v[132:135], v[36:51]
	s_waitcnt lgkmcnt(10)
	v_mfma_f32_32x32x16_bf16 v[20:35], v[84:87], v[132:135], v[20:35]
	s_waitcnt lgkmcnt(8)
	v_mfma_f32_32x32x16_bf16 v[4:19], v[92:95], v[132:135], v[4:19]
	s_waitcnt lgkmcnt(6)
	v_mfma_f32_32x32x16_bf16 v[52:67], v[72:75], v[136:139], v[52:67]
	s_waitcnt lgkmcnt(4)
	v_mfma_f32_32x32x16_bf16 v[36:51], v[80:83], v[136:139], v[36:51]
	s_waitcnt lgkmcnt(2)
	v_mfma_f32_32x32x16_bf16 v[20:35], v[88:91], v[136:139], v[20:35]
	s_waitcnt lgkmcnt(0)
	v_mfma_f32_32x32x16_bf16 v[4:19], v[96:99], v[136:139], v[4:19]
